# baseline (speedup 1.0000x reference)
_Z10attn64_fwdPKDF16_S0_S0_PDF16_:
	v_readfirstlane_b32 s3, v0
	s_cmpk_lt_i32 s3, 0x100
	s_cbranch_scc1 .LBB1_2
	s_nop 0
